# barrier rewrite plus an early L2 write-back by the middle arriver of each XCD
# baseline (speedup 1.0000x reference)
.LBB0_70:
	v_readlane_b32 s2, v253, 36
	s_lshl_b32 s2, s2, 8
	v_readlane_b32 s4, v253, 34
	v_readlane_b32 s5, v253, 35
	s_add_u32 s2, s4, s2
	s_addc_u32 s3, s5, 0
	v_mov_b32_e32 v2, 0x1000
	v_mov_b32_e32 v4, 1
	global_atomic_add v4, v2, v4, s[2:3] offset:1024 sc0
	v_cvt_f32_u32_e32 v2, v3
	v_sub_u32_e32 v5, 0, v3
	v_rcp_iflag_f32_e32 v2, v2
	s_nop 0
	v_mul_f32_e32 v2, 0x4f7ffffe, v2
	v_cvt_u32_f32_e32 v2, v2
	v_mul_lo_u32 v5, v5, v2
	v_mul_hi_u32 v5, v2, v5
	v_add_u32_e32 v2, v2, v5
	s_waitcnt vmcnt(0)
	v_mul_hi_u32 v2, v4, v2
	v_mul_lo_u32 v5, v2, v3
	v_sub_u32_e32 v5, v4, v5
	v_add_u32_e32 v6, 1, v2
	v_cmp_ge_u32_e32 vcc, v5, v3
	v_add_u32_e32 v4, 1, v4
	s_nop 0
	v_cndmask_b32_e32 v2, v2, v6, vcc
	v_sub_u32_e32 v6, v5, v3
	v_cndmask_b32_e32 v5, v5, v6, vcc
	v_add_u32_e32 v6, 1, v2
	v_cmp_ge_u32_e32 vcc, v5, v3
	s_nop 1
	v_cndmask_b32_e32 v2, v2, v6, vcc
	v_mul_lo_u32 v5, v3, v2
	v_add_u32_e32 v3, v5, v3
	v_cmp_ne_u32_e32 vcc, v4, v3
	s_and_saveexec_b64 s[4:5], vcc
	s_xor_b64 s[4:5], exec, s[4:5]
	s_cbranch_execz .LBB0_84
	s_waitcnt lgkmcnt(0)
	v_sub_u32_e32 v4, v4, v5
	v_sub_u32_e32 v6, v3, v5
	v_mul_u32_u24_e32 v6, 4, v6
	v_lshrrev_b32_e32 v6, 3, v6
	v_cmp_eq_u32_e32 vcc, v6, v4
	s_cbranch_vccz .Lxbp_0
	buffer_wbl2 sc1
.Lxbp_0:
	buffer_inv sc1
	v_mad_u32_u24 v3, v2, v1, v1
	v_mov_b32_e32 v4, 0x2000
	s_mov_b32 s26, 0

.Lxbp_1:
	buffer_inv sc1
	v_mad_u32_u24 v3, v2, v1, v1
	v_mov_b32_e32 v4, 0x2000
	s_mov_b32 s22, 0

.LBB0_959:
	v_readlane_b32 s4, v253, 36
	s_lshl_b32 s4, s4, 8
	v_readlane_b32 s6, v253, 34
	v_readlane_b32 s7, v253, 35
	s_add_u32 s4, s6, s4
	s_addc_u32 s5, s7, 0
	v_mov_b32_e32 v2, 0x1000
	v_mov_b32_e32 v4, 1
	global_atomic_add v4, v2, v4, s[4:5] offset:1024 sc0
	v_cvt_f32_u32_e32 v2, v3
	v_sub_u32_e32 v5, 0, v3
	v_rcp_iflag_f32_e32 v2, v2
	s_nop 0
	v_mul_f32_e32 v2, 0x4f7ffffe, v2
	v_cvt_u32_f32_e32 v2, v2
	v_mul_lo_u32 v5, v5, v2
	v_mul_hi_u32 v5, v2, v5
	v_add_u32_e32 v2, v2, v5
	s_waitcnt vmcnt(0)
	v_mul_hi_u32 v2, v4, v2
	v_mul_lo_u32 v5, v2, v3
	v_sub_u32_e32 v5, v4, v5
	v_add_u32_e32 v6, 1, v2
	v_cmp_ge_u32_e32 vcc, v5, v3
	v_add_u32_e32 v4, 1, v4
	s_nop 0
	v_cndmask_b32_e32 v2, v2, v6, vcc
	v_sub_u32_e32 v6, v5, v3
	v_cndmask_b32_e32 v5, v5, v6, vcc
	v_add_u32_e32 v6, 1, v2
	v_cmp_ge_u32_e32 vcc, v5, v3
	s_nop 1
	v_cndmask_b32_e32 v2, v2, v6, vcc
	v_mul_lo_u32 v5, v3, v2
	v_add_u32_e32 v3, v5, v3
	v_cmp_ne_u32_e32 vcc, v4, v3
	s_and_saveexec_b64 s[6:7], vcc
	s_xor_b64 s[6:7], exec, s[6:7]
	s_cbranch_execz .LBB0_973
	s_waitcnt lgkmcnt(0)
	v_sub_u32_e32 v4, v4, v5
	v_sub_u32_e32 v6, v3, v5
	v_mul_u32_u24_e32 v6, 4, v6
	v_lshrrev_b32_e32 v6, 3, v6
	v_cmp_eq_u32_e32 vcc, v6, v4
	s_cbranch_vccz .Lxbp_6
	buffer_wbl2 sc1
.Lxbp_6:
	buffer_inv sc1
	v_mad_u32_u24 v3, v2, v1, v1
	v_mov_b32_e32 v4, 0x2000
	s_mov_b32 s24, 0

.LBB0_1572:
	v_readlane_b32 s2, v253, 36
	s_lshl_b32 s2, s2, 8
	v_readlane_b32 s4, v253, 34
	v_readlane_b32 s5, v253, 35
	s_add_u32 s2, s4, s2
	s_addc_u32 s3, s5, 0
	v_mov_b32_e32 v3, 0x1000
	v_mov_b32_e32 v5, 1
	global_atomic_add v5, v3, v5, s[2:3] offset:1024 sc0
	v_cvt_f32_u32_e32 v3, v4
	v_sub_u32_e32 v6, 0, v4
	v_rcp_iflag_f32_e32 v3, v3
	s_nop 0
	v_mul_f32_e32 v3, 0x4f7ffffe, v3
	v_cvt_u32_f32_e32 v3, v3
	v_mul_lo_u32 v6, v6, v3
	v_mul_hi_u32 v6, v3, v6
	v_add_u32_e32 v3, v3, v6
	s_waitcnt vmcnt(0)
	v_mul_hi_u32 v3, v5, v3
	v_mul_lo_u32 v6, v3, v4
	v_sub_u32_e32 v6, v5, v6
	v_add_u32_e32 v7, 1, v3
	v_cmp_ge_u32_e32 vcc, v6, v4
	v_add_u32_e32 v5, 1, v5
	s_nop 0
	v_cndmask_b32_e32 v3, v3, v7, vcc
	v_sub_u32_e32 v7, v6, v4
	v_cndmask_b32_e32 v6, v6, v7, vcc
	v_add_u32_e32 v7, 1, v3
	v_cmp_ge_u32_e32 vcc, v6, v4
	s_nop 1
	v_cndmask_b32_e32 v3, v3, v7, vcc
	v_mul_lo_u32 v6, v4, v3
	v_add_u32_e32 v4, v6, v4
	v_cmp_ne_u32_e32 vcc, v5, v4
	s_and_saveexec_b64 s[4:5], vcc
	s_xor_b64 s[4:5], exec, s[4:5]
	s_cbranch_execz .LBB0_1586
	s_waitcnt lgkmcnt(0)
	v_sub_u32_e32 v5, v5, v6
	v_sub_u32_e32 v7, v4, v6
	v_mul_u32_u24_e32 v7, 4, v7
	v_lshrrev_b32_e32 v7, 3, v7
	v_cmp_eq_u32_e32 vcc, v7, v5
	s_cbranch_vccz .Lxbp_11
	buffer_wbl2 sc1
.Lxbp_11:
	buffer_inv sc1
	v_mad_u32_u24 v4, v3, v2, v2
	v_mov_b32_e32 v5, 0x2000
	s_mov_b32 s22, 0

.LBB0_1790:
	v_readlane_b32 s4, v253, 36
	s_lshl_b32 s4, s4, 8
	v_readlane_b32 s6, v253, 34
	v_readlane_b32 s7, v253, 35
	s_add_u32 s4, s6, s4
	s_addc_u32 s5, s7, 0
	v_mov_b32_e32 v3, 0x1000
	v_mov_b32_e32 v5, 1
	global_atomic_add v5, v3, v5, s[4:5] offset:1024 sc0
	v_cvt_f32_u32_e32 v3, v4
	v_sub_u32_e32 v6, 0, v4
	v_rcp_iflag_f32_e32 v3, v3
	s_nop 0
	v_mul_f32_e32 v3, 0x4f7ffffe, v3
	v_cvt_u32_f32_e32 v3, v3
	v_mul_lo_u32 v6, v6, v3
	v_mul_hi_u32 v6, v3, v6
	v_add_u32_e32 v3, v3, v6
	s_waitcnt vmcnt(0)
	v_mul_hi_u32 v3, v5, v3
	v_mul_lo_u32 v6, v3, v4
	v_sub_u32_e32 v6, v5, v6
	v_add_u32_e32 v7, 1, v3
	v_cmp_ge_u32_e32 vcc, v6, v4
	v_add_u32_e32 v5, 1, v5
	s_nop 0
	v_cndmask_b32_e32 v3, v3, v7, vcc
	v_sub_u32_e32 v7, v6, v4
	v_cndmask_b32_e32 v6, v6, v7, vcc
	v_add_u32_e32 v7, 1, v3
	v_cmp_ge_u32_e32 vcc, v6, v4
	s_nop 1
	v_cndmask_b32_e32 v3, v3, v7, vcc
	v_mul_lo_u32 v6, v4, v3
	v_add_u32_e32 v4, v6, v4
	v_cmp_ne_u32_e32 vcc, v5, v4
	s_and_saveexec_b64 s[6:7], vcc
	s_xor_b64 s[6:7], exec, s[6:7]
	s_cbranch_execz .LBB0_1804
	s_waitcnt lgkmcnt(0)
	v_sub_u32_e32 v5, v5, v6
	v_sub_u32_e32 v7, v4, v6
	v_mul_u32_u24_e32 v7, 4, v7
	v_lshrrev_b32_e32 v7, 3, v7
	v_cmp_eq_u32_e32 vcc, v7, v5
	s_cbranch_vccz .Lxbp_13
	buffer_wbl2 sc1
.Lxbp_13:
	buffer_inv sc1
	v_mad_u32_u24 v4, v3, v2, v2
	v_mov_b32_e32 v5, 0x2000
	s_mov_b32 s26, 0

.Lxbp_14:
	buffer_inv sc1
	v_mad_u32_u24 v4, v3, v2, v2
	v_mov_b32_e32 v5, 0x2000
	s_mov_b32 s24, 0
